# grid barrier: buffer_inv sc1 hoisted to arrival (overlaps arrive atomic), removed from post-release path
# speedup vs baseline: 1.0137x; 1.0137x over previous
.LBB0_188:
	s_mov_b64 s[4:5], exec
	v_readlane_b32 s2, v254, 38
	s_lshl_b32 s2, s2, 8
	v_mbcnt_lo_u32_b32 v1, s4, 0
	s_add_u32 s2, s72, s2
	v_mbcnt_hi_u32_b32 v1, s5, v1
	s_addc_u32 s3, s73, 0
	v_cmp_eq_u32_e32 vcc, 0, v1
	s_and_saveexec_b64 s[6:7], vcc
	s_cbranch_execz .LBB0_190
	s_bcnt1_i32_b64 s4, s[4:5]
	v_mov_b32_e32 v3, 0x1000
	v_mov_b32_e32 v4, s4
	buffer_inv sc1
	global_atomic_add v3, v3, v4, s[2:3] offset:1024 sc0

.LBB0_203:
	s_or_b64 exec, exec, s[6:7]
	s_waitcnt vmcnt(0)
	s_waitcnt vmcnt(0)

.LBB0_221:
	s_or_b64 exec, exec, s[4:5]
	s_mov_b64 s[4:5], exec
	v_mbcnt_lo_u32_b32 v0, s4, 0
	v_mbcnt_hi_u32_b32 v0, s5, v0
	v_cmp_eq_u32_e32 vcc, 0, v0
	s_waitcnt vmcnt(0)
	s_and_saveexec_b64 s[6:7], vcc
	s_cbranch_execz .LBB0_223
	s_bcnt1_i32_b64 s4, s[4:5]
	v_mov_b32_e32 v0, 0x2000
	v_mov_b32_e32 v1, s4
	global_atomic_add v0, v1, s[2:3] offset:1024

.LBB0_264:
	s_mov_b64 s[6:7], exec
	v_readlane_b32 s2, v254, 38
	s_lshl_b32 s2, s2, 8
	v_mbcnt_lo_u32_b32 v1, s6, 0
	s_add_u32 s2, s72, s2
	v_mbcnt_hi_u32_b32 v1, s7, v1
	s_addc_u32 s3, s73, 0
	v_cmp_eq_u32_e32 vcc, 0, v1
	s_and_saveexec_b64 s[8:9], vcc
	s_cbranch_execz .LBB0_266
	s_bcnt1_i32_b64 s6, s[6:7]
	v_mov_b32_e32 v3, 0x1000
	v_mov_b32_e32 v4, s6
	buffer_inv sc1
	global_atomic_add v3, v3, v4, s[2:3] offset:1024 sc0

.LBB0_279:
	s_or_b64 exec, exec, s[8:9]
	s_waitcnt vmcnt(0)
	s_waitcnt vmcnt(0)

.LBB0_297:
	s_or_b64 exec, exec, s[6:7]
	s_mov_b64 s[6:7], exec
	v_mbcnt_lo_u32_b32 v0, s6, 0
	v_mbcnt_hi_u32_b32 v0, s7, v0
	v_cmp_eq_u32_e32 vcc, 0, v0
	s_waitcnt vmcnt(0)
	s_and_saveexec_b64 s[8:9], vcc
	s_cbranch_execz .LBB0_299
	s_bcnt1_i32_b64 s6, s[6:7]
	v_mov_b32_e32 v0, 0x2000
	v_mov_b32_e32 v1, s6
	global_atomic_add v0, v1, s[2:3] offset:1024

.LBB0_856:
	s_mov_b64 s[4:5], exec
	v_readlane_b32 s2, v254, 38
	s_lshl_b32 s2, s2, 8
	v_mbcnt_lo_u32_b32 v1, s4, 0
	s_add_u32 s2, s72, s2
	v_mbcnt_hi_u32_b32 v1, s5, v1
	s_addc_u32 s3, s73, 0
	v_cmp_eq_u32_e32 vcc, 0, v1
	s_and_saveexec_b64 s[12:13], vcc
	s_cbranch_execz .LBB0_858
	s_bcnt1_i32_b64 s4, s[4:5]
	v_mov_b32_e32 v3, 0x1000
	v_mov_b32_e32 v4, s4
	buffer_inv sc1
	global_atomic_add v3, v3, v4, s[2:3] offset:1024 sc0

.LBB0_871:
	s_or_b64 exec, exec, s[12:13]
	s_waitcnt vmcnt(0)
	s_waitcnt vmcnt(0)

.LBB0_889:
	s_or_b64 exec, exec, s[4:5]
	s_mov_b64 s[4:5], exec
	v_mbcnt_lo_u32_b32 v0, s4, 0
	v_mbcnt_hi_u32_b32 v0, s5, v0
	v_cmp_eq_u32_e32 vcc, 0, v0
	s_waitcnt vmcnt(0)
	s_and_saveexec_b64 s[12:13], vcc
	s_cbranch_execz .LBB0_891
	s_bcnt1_i32_b64 s4, s[4:5]
	v_mov_b32_e32 v0, 0x2000
	v_mov_b32_e32 v1, s4
	global_atomic_add v0, v1, s[2:3] offset:1024

.LBB0_946:
	s_mov_b64 s[6:7], exec
	v_readlane_b32 s4, v254, 38
	s_lshl_b32 s4, s4, 8
	v_mbcnt_lo_u32_b32 v1, s6, 0
	s_add_u32 s4, s72, s4
	v_mbcnt_hi_u32_b32 v1, s7, v1
	s_addc_u32 s5, s73, 0
	v_cmp_eq_u32_e32 vcc, 0, v1
	s_and_saveexec_b64 s[12:13], vcc
	s_cbranch_execz .LBB0_948
	s_bcnt1_i32_b64 s6, s[6:7]
	v_mov_b32_e32 v3, 0x1000
	v_mov_b32_e32 v4, s6
	buffer_inv sc1
	global_atomic_add v3, v3, v4, s[4:5] offset:1024 sc0

.LBB0_979:
	s_or_b64 exec, exec, s[6:7]
	s_mov_b64 s[6:7], exec
	v_mbcnt_lo_u32_b32 v0, s6, 0
	v_mbcnt_hi_u32_b32 v0, s7, v0
	v_cmp_eq_u32_e32 vcc, 0, v0
	s_waitcnt vmcnt(0)
	s_and_saveexec_b64 s[12:13], vcc
	s_cbranch_execz .LBB0_981
	s_bcnt1_i32_b64 s6, s[6:7]
	v_mov_b32_e32 v0, 0x2000
	v_mov_b32_e32 v1, s6
	global_atomic_add v0, v1, s[4:5] offset:1024

.LBB0_1733:
	s_mov_b64 s[4:5], exec
	v_readlane_b32 s2, v254, 38
	s_lshl_b32 s2, s2, 8
	v_mbcnt_lo_u32_b32 v1, s4, 0
	s_add_u32 s2, s72, s2
	v_mbcnt_hi_u32_b32 v1, s5, v1
	s_addc_u32 s3, s73, 0
	v_cmp_eq_u32_e32 vcc, 0, v1
	s_and_saveexec_b64 s[8:9], vcc
	s_cbranch_execz .LBB0_1735
	s_bcnt1_i32_b64 s4, s[4:5]
	v_mov_b32_e32 v3, 0x1000
	v_mov_b32_e32 v4, s4
	buffer_inv sc1
	global_atomic_add v3, v3, v4, s[2:3] offset:1024 sc0

.LBB0_1766:
	s_or_b64 exec, exec, s[4:5]
	s_mov_b64 s[4:5], exec
	v_mbcnt_lo_u32_b32 v0, s4, 0
	v_mbcnt_hi_u32_b32 v0, s5, v0
	v_cmp_eq_u32_e32 vcc, 0, v0
	s_waitcnt vmcnt(0)
	s_and_saveexec_b64 s[8:9], vcc
	s_cbranch_execz .LBB0_1768
	s_bcnt1_i32_b64 s4, s[4:5]
	v_mov_b32_e32 v0, 0x2000
	v_mov_b32_e32 v1, s4
	global_atomic_add v0, v1, s[2:3] offset:1024

.LBB0_1823:
	s_mov_b64 s[6:7], exec
	v_readlane_b32 s4, v254, 38
	s_lshl_b32 s4, s4, 8
	v_mbcnt_lo_u32_b32 v1, s6, 0
	s_add_u32 s4, s72, s4
	v_mbcnt_hi_u32_b32 v1, s7, v1
	s_addc_u32 s5, s73, 0
	v_cmp_eq_u32_e32 vcc, 0, v1
	s_and_saveexec_b64 s[8:9], vcc
	s_cbranch_execz .LBB0_1825
	s_bcnt1_i32_b64 s6, s[6:7]
	v_mov_b32_e32 v3, 0x1000
	v_mov_b32_e32 v4, s6
	buffer_inv sc1
	global_atomic_add v3, v3, v4, s[4:5] offset:1024 sc0

.LBB0_1856:
	s_or_b64 exec, exec, s[6:7]
	s_mov_b64 s[6:7], exec
	v_mbcnt_lo_u32_b32 v0, s6, 0
	v_mbcnt_hi_u32_b32 v0, s7, v0
	v_cmp_eq_u32_e32 vcc, 0, v0
	s_waitcnt vmcnt(0)
	s_and_saveexec_b64 s[8:9], vcc
	s_cbranch_execz .LBB0_1858
	s_bcnt1_i32_b64 s6, s[6:7]
	v_mov_b32_e32 v0, 0x2000
	v_mov_b32_e32 v1, s6
	global_atomic_add v0, v1, s[4:5] offset:1024
